# v10_ffn1pipe
# baseline (speedup 1.0000x reference)
.LBB1_139:
	s_waitcnt vmcnt(5) lgkmcnt(7)
	v_mfma_f32_32x32x16_f16 v[50:65], v[100:103], v[168:171], v[18:33]
	s_waitcnt vmcnt(3)
	v_mfma_f32_32x32x16_f16 v[34:49], v[128:131], v[168:171], v[2:17]
	s_waitcnt lgkmcnt(6)
	v_mfma_f32_32x32x16_f16 v[50:65], v[92:95], v[164:167], v[50:65]
	v_mfma_f32_32x32x16_f16 v[34:49], v[124:127], v[164:167], v[34:49]
	s_waitcnt lgkmcnt(5)
	v_mfma_f32_32x32x16_f16 v[50:65], v[88:91], v[160:163], v[50:65]
	v_mfma_f32_32x32x16_f16 v[34:49], v[120:123], v[160:163], v[34:49]
	s_waitcnt lgkmcnt(4)
	v_mfma_f32_32x32x16_f16 v[50:65], v[80:83], v[156:159], v[50:65]
	v_mfma_f32_32x32x16_f16 v[34:49], v[112:115], v[156:159], v[34:49]
	s_waitcnt lgkmcnt(3)
	v_mfma_f32_32x32x16_f16 v[50:65], v[96:99], v[152:155], v[50:65]
	v_mfma_f32_32x32x16_f16 v[34:49], v[116:119], v[152:155], v[34:49]
	s_waitcnt lgkmcnt(2)
	v_mfma_f32_32x32x16_f16 v[50:65], v[84:87], v[148:151], v[50:65]
	v_mfma_f32_32x32x16_f16 v[34:49], v[108:111], v[148:151], v[34:49]
	s_waitcnt lgkmcnt(1)
	v_mfma_f32_32x32x16_f16 v[50:65], v[76:79], v[144:147], v[50:65]
	v_mfma_f32_32x32x16_f16 v[34:49], v[104:107], v[144:147], v[34:49]
	v_cndmask_b32_e64 v144, 0, 1, s[2:3]
	s_add_i32 s2, s30, 32
	v_cmp_ne_u32_e32 vcc, 1, v144
	s_waitcnt lgkmcnt(0)
	v_mfma_f32_32x32x16_f16 v[50:65], v[68:71], v[140:143], v[50:65]
	v_mfma_f32_32x32x16_f16 v[34:49], v[72:75], v[140:143], v[34:49]
	v_or_b32_e32 v140, s2, v1
	v_min_i32_e32 v140, 0x53, v140
	v_mad_u32_u24 v140, v140, s64, v204
	ds_read_b128 v[168:171], v140 offset:43008
	ds_read_b128 v[164:167], v140 offset:43040
	ds_read_b128 v[160:163], v140 offset:43072
	ds_read_b128 v[156:159], v140 offset:43104
	ds_read_b128 v[152:155], v140 offset:43136
	ds_read_b128 v[148:151], v140 offset:43168
	ds_read_b128 v[144:147], v140 offset:43200
	ds_read_b128 v[140:143], v140 offset:43232
	v_or_b32_e32 v211, s30, v1
	v_cvt_pk_f16_f32 v50, v50, v51
	v_cvt_pk_f16_f32 v51, v52, v53
	v_cvt_pk_f16_f32 v34, v34, v35
	v_cvt_pk_f16_f32 v35, v36, v37
	v_cvt_pk_f16_f32 v36, v54, v55
	v_cvt_pk_f16_f32 v37, v56, v57
	v_cvt_pk_f16_f32 v38, v38, v39
	v_cvt_pk_f16_f32 v39, v40, v41
	v_mad_u32_u24 v211, v211, s69, v239
	v_pk_max_f16 v50, v50, 0
	v_pk_max_f16 v51, v51, 0
	v_pk_max_f16 v34, v34, 0
	v_pk_max_f16 v35, v35, 0
	v_pk_max_f16 v36, v36, 0
	v_pk_max_f16 v37, v37, 0
	v_pk_max_f16 v38, v38, 0
	v_pk_max_f16 v39, v39, 0
	ds_write2_b64 v211, v[50:51], v[36:37] offset1:2
	ds_write2_b64 v211, v[34:35], v[38:39] offset0:8 offset1:10
	v_cvt_pk_f16_f32 v34, v58, v59
	v_cvt_pk_f16_f32 v35, v60, v61
	v_cvt_pk_f16_f32 v38, v62, v63
	v_cvt_pk_f16_f32 v39, v64, v65
	v_pk_max_f16 v34, v34, 0
	v_pk_max_f16 v35, v35, 0
	v_cvt_pk_f16_f32 v36, v42, v43
	v_cvt_pk_f16_f32 v37, v44, v45
	v_pk_max_f16 v38, v38, 0
	v_pk_max_f16 v39, v39, 0
	v_cvt_pk_f16_f32 v40, v46, v47
	v_cvt_pk_f16_f32 v41, v48, v49
	v_pk_max_f16 v36, v36, 0
	v_pk_max_f16 v37, v37, 0
	v_pk_max_f16 v40, v40, 0
	v_pk_max_f16 v41, v41, 0
	ds_write2_b64 v211, v[34:35], v[38:39] offset0:4 offset1:6
	ds_write2_b64 v211, v[36:37], v[40:41] offset0:12 offset1:14
	s_mov_b64 s[2:3], 0
	s_mov_b32 s30, 32
	s_waitcnt vmcnt(5) lgkmcnt(7)
	v_mfma_f32_32x32x16_f16 v[50:65], v[100:103], v[168:171], v[18:33]
	s_waitcnt vmcnt(3)
	v_mfma_f32_32x32x16_f16 v[34:49], v[128:131], v[168:171], v[2:17]
	s_waitcnt lgkmcnt(6)
	v_mfma_f32_32x32x16_f16 v[50:65], v[92:95], v[164:167], v[50:65]
	v_mfma_f32_32x32x16_f16 v[34:49], v[124:127], v[164:167], v[34:49]
	s_waitcnt lgkmcnt(5)
	v_mfma_f32_32x32x16_f16 v[50:65], v[88:91], v[160:163], v[50:65]
	v_mfma_f32_32x32x16_f16 v[34:49], v[120:123], v[160:163], v[34:49]
	s_waitcnt lgkmcnt(4)
	v_mfma_f32_32x32x16_f16 v[50:65], v[80:83], v[156:159], v[50:65]
	v_mfma_f32_32x32x16_f16 v[34:49], v[112:115], v[156:159], v[34:49]
	s_waitcnt lgkmcnt(3)
	v_mfma_f32_32x32x16_f16 v[50:65], v[96:99], v[152:155], v[50:65]
	v_mfma_f32_32x32x16_f16 v[34:49], v[116:119], v[152:155], v[34:49]
	s_waitcnt lgkmcnt(2)
	v_mfma_f32_32x32x16_f16 v[50:65], v[84:87], v[148:151], v[50:65]
	v_mfma_f32_32x32x16_f16 v[34:49], v[108:111], v[148:151], v[34:49]
	s_waitcnt lgkmcnt(1)
	v_mfma_f32_32x32x16_f16 v[50:65], v[76:79], v[144:147], v[50:65]
	v_mfma_f32_32x32x16_f16 v[34:49], v[104:107], v[144:147], v[34:49]
	v_cndmask_b32_e64 v144, 0, 1, s[2:3]
	s_add_i32 s2, s30, 32
	v_cmp_ne_u32_e32 vcc, 1, v144
	s_waitcnt lgkmcnt(0)
	v_mfma_f32_32x32x16_f16 v[50:65], v[68:71], v[140:143], v[50:65]
	v_mfma_f32_32x32x16_f16 v[34:49], v[72:75], v[140:143], v[34:49]
	v_or_b32_e32 v140, s2, v1
	v_min_i32_e32 v140, 0x53, v140
	v_mad_u32_u24 v140, v140, s64, v204
	ds_read_b128 v[168:171], v140 offset:43008
	ds_read_b128 v[164:167], v140 offset:43040
	ds_read_b128 v[160:163], v140 offset:43072
	ds_read_b128 v[156:159], v140 offset:43104
	ds_read_b128 v[152:155], v140 offset:43136
	ds_read_b128 v[148:151], v140 offset:43168
	ds_read_b128 v[144:147], v140 offset:43200
	ds_read_b128 v[140:143], v140 offset:43232
	s_waitcnt lgkmcnt(7)
	v_mfma_f32_32x32x16_f16 v[18:33], v[100:103], v[168:171], v[18:33]
	v_or_b32_e32 v211, s30, v1
	v_cvt_pk_f16_f32 v50, v50, v51
	v_cvt_pk_f16_f32 v51, v52, v53
	s_waitcnt lgkmcnt(6)
	v_mfma_f32_32x32x16_f16 v[18:33], v[92:95], v[164:167], v[18:33]
	v_cvt_pk_f16_f32 v34, v34, v35
	v_cvt_pk_f16_f32 v35, v36, v37
	v_cvt_pk_f16_f32 v36, v54, v55
	s_waitcnt lgkmcnt(5)
	v_mfma_f32_32x32x16_f16 v[18:33], v[88:91], v[160:163], v[18:33]
	v_cvt_pk_f16_f32 v37, v56, v57
	v_cvt_pk_f16_f32 v38, v38, v39
	v_cvt_pk_f16_f32 v39, v40, v41
	s_waitcnt lgkmcnt(4)
	v_mfma_f32_32x32x16_f16 v[18:33], v[80:83], v[156:159], v[18:33]
	v_mad_u32_u24 v211, v211, s69, v239
	v_pk_max_f16 v50, v50, 0
	v_pk_max_f16 v51, v51, 0
	s_waitcnt lgkmcnt(3)
	v_mfma_f32_32x32x16_f16 v[18:33], v[96:99], v[152:155], v[18:33]
	v_pk_max_f16 v34, v34, 0
	v_pk_max_f16 v35, v35, 0
	v_pk_max_f16 v36, v36, 0
	s_waitcnt lgkmcnt(2)
	v_mfma_f32_32x32x16_f16 v[18:33], v[84:87], v[148:151], v[18:33]
	v_pk_max_f16 v37, v37, 0
	v_pk_max_f16 v38, v38, 0
	v_pk_max_f16 v39, v39, 0
	s_waitcnt lgkmcnt(1)
	v_mfma_f32_32x32x16_f16 v[18:33], v[76:79], v[144:147], v[18:33]
	ds_write2_b64 v211, v[50:51], v[36:37] offset1:2
	ds_write2_b64 v211, v[34:35], v[38:39] offset0:8 offset1:10
	v_cvt_pk_f16_f32 v34, v58, v59
	v_mfma_f32_32x32x16_f16 v[2:17], v[128:131], v[168:171], v[2:17]
	v_cvt_pk_f16_f32 v35, v60, v61
	v_cvt_pk_f16_f32 v38, v62, v63
	v_cvt_pk_f16_f32 v39, v64, v65
	v_mfma_f32_32x32x16_f16 v[2:17], v[124:127], v[164:167], v[2:17]
	v_pk_max_f16 v34, v34, 0
	v_pk_max_f16 v35, v35, 0
	v_mfma_f32_32x32x16_f16 v[2:17], v[120:123], v[160:163], v[2:17]
	v_cvt_pk_f16_f32 v36, v42, v43
	v_cvt_pk_f16_f32 v37, v44, v45
	v_mfma_f32_32x32x16_f16 v[2:17], v[112:115], v[156:159], v[2:17]
	v_pk_max_f16 v38, v38, 0
	v_pk_max_f16 v39, v39, 0
	v_mfma_f32_32x32x16_f16 v[2:17], v[116:119], v[152:155], v[2:17]
	v_cvt_pk_f16_f32 v40, v46, v47
	v_cvt_pk_f16_f32 v41, v48, v49
	v_mfma_f32_32x32x16_f16 v[2:17], v[108:111], v[148:151], v[2:17]
	v_pk_max_f16 v36, v36, 0
	v_pk_max_f16 v37, v37, 0
	v_mfma_f32_32x32x16_f16 v[2:17], v[104:107], v[144:147], v[2:17]
	v_pk_max_f16 v40, v40, 0
	v_pk_max_f16 v41, v41, 0
	s_waitcnt lgkmcnt(0)
	v_mfma_f32_32x32x16_f16 v[18:33], v[68:71], v[140:143], v[18:33]
	ds_write2_b64 v211, v[34:35], v[38:39] offset0:4 offset1:6
	ds_write2_b64 v211, v[36:37], v[40:41] offset0:12 offset1:14
	v_mfma_f32_32x32x16_f16 v[2:17], v[72:75], v[140:143], v[2:17]
	v_add_co_u32_e32 v34, vcc, 0x1000, v174
	s_nop 1
	v_addc_co_u32_e32 v35, vcc, 0, v175, vcc
	global_load_dwordx4 v[80:83], v[174:175], off offset:2048
	global_load_dwordx4 v[76:79], v[174:175], off offset:3072
	global_load_dwordx4 v[62:65], v[34:35], off
	global_load_dwordx4 v[58:61], v[34:35], off offset:1024
	global_load_dwordx4 v[54:57], v[34:35], off offset:2048
	global_load_dwordx4 v[50:53], v[34:35], off offset:3072
	s_and_saveexec_b64 s[2:3], s[12:13]
	s_cbranch_execz .LBB1_142
	s_nop 8
	v_cvt_pk_f16_f32 v18, v18, v19
	v_cvt_pk_f16_f32 v19, v20, v21
	v_cvt_pk_f16_f32 v2, v2, v3
	v_cvt_pk_f16_f32 v3, v4, v5
	v_cvt_pk_f16_f32 v4, v22, v23
	v_cvt_pk_f16_f32 v5, v24, v25
	v_cvt_pk_f16_f32 v6, v6, v7
	v_cvt_pk_f16_f32 v7, v8, v9
	v_pk_max_f16 v18, v18, 0
	v_pk_max_f16 v19, v19, 0
	v_pk_max_f16 v2, v2, 0
	v_pk_max_f16 v3, v3, 0
	v_pk_max_f16 v4, v4, 0
	v_pk_max_f16 v5, v5, 0
	v_pk_max_f16 v6, v6, 0
	v_pk_max_f16 v7, v7, 0
	ds_write2_b64 v244, v[18:19], v[4:5] offset1:2
	ds_write2_b64 v244, v[2:3], v[6:7] offset0:8 offset1:10
	v_cvt_pk_f16_f32 v2, v26, v27
	v_cvt_pk_f16_f32 v3, v28, v29
	v_cvt_pk_f16_f32 v6, v30, v31
	v_cvt_pk_f16_f32 v7, v32, v33
	v_pk_max_f16 v2, v2, 0
	v_pk_max_f16 v3, v3, 0
	v_cvt_pk_f16_f32 v4, v10, v11
	v_cvt_pk_f16_f32 v5, v12, v13
	v_pk_max_f16 v6, v6, 0
	v_pk_max_f16 v7, v7, 0
	v_cvt_pk_f16_f32 v8, v14, v15
	v_cvt_pk_f16_f32 v9, v16, v17
	v_pk_max_f16 v4, v4, 0
	v_pk_max_f16 v5, v5, 0
	v_pk_max_f16 v8, v8, 0
	v_pk_max_f16 v9, v9, 0
	ds_write2_b64 v244, v[2:3], v[6:7] offset0:4 offset1:6
	ds_write2_b64 v244, v[4:5], v[8:9] offset0:12 offset1:14
